# v55 + MLA loop: lazy-rescale decision as a wave-uniform branch (alpha = 1 fast path; new-max / exp2 / selects out of line)
# baseline (speedup 1.0000x reference)
.LBB0_861:
	ds_read_b128 v[96:99], v209 offset:49152
	ds_read_b128 v[100:103], v209 offset:57344
	ds_read_b128 v[162:165], v211 offset:49152
	ds_read_b128 v[166:169], v211 offset:57344
	s_add_i32 s2, 0, 0x12000
	v_add_u32_e32 v233, s2, v218
	s_waitcnt lgkmcnt(3)
	v_mfma_f32_32x32x16_bf16 v[112:127], v[96:99], v[158:161], 0
	v_add_u32_e32 v234, s2, v220
	v_add_u32_e32 v236, s2, v222
	v_add_u32_e32 v235, s2, v224
	v_exp_f32_e32 v80, v80
	v_exp_f32_e32 v81, v81
	v_exp_f32_e32 v82, v82
	v_exp_f32_e32 v83, v83
	s_waitcnt lgkmcnt(2)
	v_mfma_f32_32x32x16_bf16 v[96:111], v[100:103], v[158:161], 0
	v_exp_f32_e32 v84, v84
	v_exp_f32_e32 v92, v92
	v_exp_f32_e32 v85, v85
	v_exp_f32_e32 v93, v93
	v_exp_f32_e32 v86, v86
	v_exp_f32_e32 v94, v94
	v_exp_f32_e32 v87, v87
	s_waitcnt lgkmcnt(1)
	v_mfma_f32_32x32x16_bf16 v[112:127], v[162:165], v[154:157], v[112:127]
	v_exp_f32_e32 v95, v95
	s_waitcnt lgkmcnt(0)
	v_mfma_f32_32x32x16_bf16 v[96:111], v[166:169], v[154:157], v[96:111]
	ds_read_b128 v[162:165], v212 offset:49152
	ds_read_b128 v[166:169], v212 offset:57344
	s_waitcnt lgkmcnt(1)
	v_mfma_f32_32x32x16_bf16 v[112:127], v[162:165], v[150:153], v[112:127]
	s_waitcnt lgkmcnt(0)
	v_mfma_f32_32x32x16_bf16 v[96:111], v[166:169], v[150:153], v[96:111]
	ds_read_b128 v[162:165], v213 offset:49152
	ds_read_b128 v[166:169], v213 offset:57344
	s_waitcnt lgkmcnt(1)
	v_mfma_f32_32x32x16_bf16 v[112:127], v[162:165], v[146:149], v[112:127]
	s_waitcnt lgkmcnt(0)
	v_mfma_f32_32x32x16_bf16 v[96:111], v[166:169], v[146:149], v[96:111]
	ds_read_b128 v[162:165], v215 offset:49152
	ds_read_b128 v[166:169], v215 offset:57344
	s_waitcnt lgkmcnt(1)
	v_mfma_f32_32x32x16_bf16 v[112:127], v[162:165], v[142:145], v[112:127]
	s_waitcnt lgkmcnt(0)
	v_mfma_f32_32x32x16_bf16 v[96:111], v[166:169], v[142:145], v[96:111]
	ds_read_b128 v[162:165], v217 offset:49152
	ds_read_b128 v[166:169], v217 offset:57344
	s_waitcnt lgkmcnt(1)
	v_mfma_f32_32x32x16_bf16 v[112:127], v[162:165], v[138:141], v[112:127]
	s_waitcnt lgkmcnt(0)
	v_mfma_f32_32x32x16_bf16 v[96:111], v[166:169], v[138:141], v[96:111]
	ds_read_b128 v[162:165], v214 offset:49152
	ds_read_b128 v[166:169], v214 offset:57344
	s_waitcnt lgkmcnt(1)
	v_mfma_f32_32x32x16_bf16 v[112:127], v[162:165], v[134:137], v[112:127]
	s_waitcnt lgkmcnt(0)
	v_mfma_f32_32x32x16_bf16 v[96:111], v[166:169], v[134:137], v[96:111]
	ds_read_b128 v[162:165], v216 offset:49152
	ds_read_b128 v[166:169], v216 offset:57344
	s_waitcnt lgkmcnt(1)
	v_mfma_f32_32x32x16_bf16 v[112:127], v[162:165], v[130:133], v[112:127]
	s_waitcnt lgkmcnt(0)
	v_mfma_f32_32x32x16_bf16 v[96:111], v[166:169], v[130:133], v[96:111]
	ds_read_b128 v[162:165], v233
	ds_read_b128 v[166:169], v233 offset:4096
	ds_read_b128 v[170:173], v204
	s_waitcnt lgkmcnt(0)
	v_mfma_f32_32x32x16_bf16 v[112:127], v[162:165], v[170:173], v[112:127]
	v_mfma_f32_32x32x16_bf16 v[96:111], v[166:169], v[170:173], v[96:111]
	ds_read_b128 v[162:165], v234
	ds_read_b128 v[166:169], v234 offset:4096
	ds_read_b128 v[170:173], v204 offset:1024
	s_waitcnt lgkmcnt(0)
	v_mfma_f32_32x32x16_bf16 v[112:127], v[162:165], v[170:173], v[112:127]
	v_mfma_f32_32x32x16_bf16 v[96:111], v[166:169], v[170:173], v[96:111]
	ds_read_b128 v[162:165], v236
	ds_read_b128 v[166:169], v236 offset:4096
	ds_read_b128 v[170:173], v204 offset:2048
	s_waitcnt lgkmcnt(0)
	v_mfma_f32_32x32x16_bf16 v[112:127], v[162:165], v[170:173], v[112:127]
	v_mfma_f32_32x32x16_bf16 v[96:111], v[166:169], v[170:173], v[96:111]
	ds_read_b128 v[162:165], v235
	ds_read_b128 v[166:169], v235 offset:4096
	ds_read_b128 v[170:173], v204 offset:3072
	s_waitcnt lgkmcnt(0)
	v_mfma_f32_32x32x16_bf16 v[112:127], v[162:165], v[170:173], v[112:127]
	v_exp_f32_e32 v162, v88
	v_exp_f32_e32 v163, v89
	v_exp_f32_e32 v164, v90
	v_exp_f32_e32 v165, v91
	v_add_f32_e32 v88, v64, v65
	v_add_f32_e32 v89, v72, v73
	v_add_f32_e32 v90, v80, v81
	v_add_f32_e32 v91, v162, v163
	v_add_f32_e32 v88, v66, v88
	v_add_f32_e32 v89, v74, v89
	v_add_f32_e32 v90, v82, v90
	v_add_f32_e32 v91, v164, v91
	v_add_f32_e32 v88, v67, v88
	v_add_f32_e32 v89, v75, v89
	v_add_f32_e32 v90, v83, v90
	v_add_f32_e32 v91, v165, v91
	v_add_f32_e32 v88, v68, v88
	v_add_f32_e32 v89, v76, v89
	v_add_f32_e32 v90, v84, v90
	v_add_f32_e32 v91, v92, v91
	v_add_f32_e32 v88, v69, v88
	v_add_f32_e32 v89, v77, v89
	v_add_f32_e32 v90, v85, v90
	v_add_f32_e32 v91, v93, v91
	v_add_f32_e32 v88, v70, v88
	v_add_f32_e32 v89, v78, v89
	v_add_f32_e32 v90, v86, v90
	v_add_f32_e32 v91, v94, v91
	v_add_f32_e32 v88, v71, v88
	v_add_f32_e32 v89, v79, v89
	v_add_f32_e32 v90, v87, v90
	v_add_f32_e32 v91, v95, v91
	v_add_f32_e32 v88, v89, v88
	v_add_f32_e32 v89, v91, v90
	v_add_f32_e32 v237, v88, v89
	v_mov_b32_e32 v238, v237
	v_cvt_pk_bf16_f32 v88, v64, v65
	v_cvt_pk_bf16_f32 v89, v66, v67
	v_cvt_pk_bf16_f32 v90, v68, v69
	v_cvt_pk_bf16_f32 v91, v70, v71
	s_nop 1
	v_permlane32_swap_b32_e32 v237, v238
	v_cvt_pk_bf16_f32 v72, v72, v73
	v_cvt_pk_bf16_f32 v73, v74, v75
	v_cvt_pk_bf16_f32 v74, v76, v77
	v_cvt_pk_bf16_f32 v75, v78, v79
	v_cvt_pk_bf16_f32 v64, v80, v81
	v_cvt_pk_bf16_f32 v65, v82, v83
	v_cvt_pk_bf16_f32 v66, v84, v85
	v_cvt_pk_bf16_f32 v67, v86, v87
	v_cvt_pk_bf16_f32 v68, v162, v163
	v_cvt_pk_bf16_f32 v69, v164, v165
	v_cvt_pk_bf16_f32 v70, v92, v93
	v_cvt_pk_bf16_f32 v71, v94, v95
	v_mfma_f32_32x32x16_bf16 v[96:111], v[166:169], v[170:173], v[96:111]
	v_lshl_add_u64 v[80:81], v[190:191], 0, s[6:7]
	global_load_dwordx4 v[162:165], v[80:81], off
	v_lshl_add_u64 v[80:81], v[192:193], 0, s[6:7]
	v_lshl_add_u64 v[76:77], v[188:189], 0, s[6:7]
	global_load_dwordx4 v[166:169], v[80:81], off
	v_lshl_add_u64 v[80:81], v[198:199], 0, s[6:7]
	global_load_dwordx4 v[76:79], v[76:77], off
	s_nop 0
	global_load_dwordx4 v[174:177], v[80:81], off
	global_load_dwordx4 v[170:173], v[186:187], off
	ds_read_b64_tr_b16 v[80:81], v201 offset:0
	ds_read_b64_tr_b16 v[82:83], v201 offset:0x800
	ds_read_b64_tr_b16 v[84:85], v201 offset:0x1000
	ds_read_b64_tr_b16 v[86:87], v201 offset:0x1800
	ds_read_b64_tr_b16 v[92:93], v201 offset:0x2000
	ds_read_b64_tr_b16 v[94:95], v201 offset:0x2800
	ds_read_b64_tr_b16 v[178:179], v201 offset:0x3000
	ds_read_b64_tr_b16 v[180:181], v201 offset:0x3800
	s_waitcnt lgkmcnt(0)
	s_nop 0
	v_mfma_f32_32x32x16_bf16 v[0:15], v[80:83], v[88:91], v[0:15]
	v_max_f32_e32 v80, v96, v97
	v_max3_f32 v81, v112, v113, v114
	v_max3_f32 v80, v80, v98, v99
	v_max3_f32 v81, v81, v115, v116
	v_max3_f32 v80, v80, v100, v101
	v_mfma_f32_32x32x16_bf16 v[0:15], v[84:87], v[72:75], v[0:15]
	v_max3_f32 v81, v81, v117, v118
	v_max3_f32 v80, v80, v102, v103
	v_max3_f32 v81, v81, v119, v120
	v_max3_f32 v80, v80, v104, v105
	v_max3_f32 v81, v81, v121, v122
	v_max3_f32 v80, v80, v106, v107
	v_max3_f32 v81, v81, v123, v124
	v_mfma_f32_32x32x16_bf16 v[0:15], v[92:95], v[64:67], v[0:15]
	v_max3_f32 v80, v80, v108, v109
	v_max3_f32 v81, v81, v125, v126
	v_max3_f32 v80, v80, v110, v111
	v_max3_f32 v194, v81, v127, v80
	ds_read_b64_tr_b16 v[80:81], v201 offset:0x200
	ds_read_b64_tr_b16 v[82:83], v201 offset:0xa00
	ds_read_b64_tr_b16 v[84:85], v201 offset:0x1200
	v_mfma_f32_32x32x16_bf16 v[0:15], v[178:181], v[68:71], v[0:15]
	ds_read_b64_tr_b16 v[86:87], v201 offset:0x1a00
	ds_read_b64_tr_b16 v[92:93], v201 offset:0x2200
	ds_read_b64_tr_b16 v[94:95], v201 offset:0x2a00
	ds_read_b64_tr_b16 v[178:179], v201 offset:0x3200
	ds_read_b64_tr_b16 v[180:181], v201 offset:0x3a00
	s_waitcnt lgkmcnt(0)
	v_mfma_f32_32x32x16_bf16 v[48:63], v[80:83], v[88:91], v[48:63]
	v_mov_b32_e32 v80, v194
	s_nop 1
	v_permlane32_swap_b32_e32 v194, v80
	v_max_f32_e32 v80, v194, v80
	v_sub_f32_e32 v81, v80, v227
	v_mfma_f32_32x32x16_bf16 v[48:63], v[84:87], v[72:75], v[48:63]
	v_cmp_ge_f32_e32 vcc, s34, v81
	v_mov_b32_e32 v202, 1.0
	s_cmp_eq_u64 vcc, exec
	s_cbranch_scc0 .Lmla_resc_0
.Lmla_resc_back_0:
	v_mfma_f32_32x32x16_bf16 v[48:63], v[92:95], v[64:67], v[48:63]
	ds_read_b64_tr_b16 v[80:81], v201 offset:0x400
	ds_read_b64_tr_b16 v[82:83], v201 offset:0xc00
	ds_read_b64_tr_b16 v[84:85], v201 offset:0x1400
	ds_read_b64_tr_b16 v[86:87], v201 offset:0x1c00
	v_mfma_f32_32x32x16_bf16 v[48:63], v[178:181], v[68:71], v[48:63]
	ds_read_b64_tr_b16 v[92:93], v201 offset:0x2400
	v_mul_f32_e32 v178, 0xbdd53b94, v227
	ds_read_b64_tr_b16 v[94:95], v201 offset:0x2c00
	v_fmamk_f32 v179, v112, 0x3dd53b94, v178
	v_fmamk_f32 v180, v113, 0x3dd53b94, v178
	ds_read_b64_tr_b16 v[112:113], v201 offset:0x3400
	v_fmamk_f32 v181, v114, 0x3dd53b94, v178
	v_fmamk_f32 v194, v115, 0x3dd53b94, v178
	ds_read_b64_tr_b16 v[114:115], v201 offset:0x3c00
	s_waitcnt lgkmcnt(0)
	v_fmamk_f32 v195, v116, 0x3dd53b94, v178
	v_fmamk_f32 v196, v117, 0x3dd53b94, v178
	v_fmamk_f32 v197, v118, 0x3dd53b94, v178
	v_fmamk_f32 v200, v119, 0x3dd53b94, v178
	v_fmamk_f32 v239, v120, 0x3dd53b94, v178
	v_fmamk_f32 v240, v121, 0x3dd53b94, v178
	v_fmamk_f32 v241, v122, 0x3dd53b94, v178
	v_fmamk_f32 v242, v123, 0x3dd53b94, v178
	v_fmamk_f32 v243, v124, 0x3dd53b94, v178
	v_fmamk_f32 v244, v125, 0x3dd53b94, v178
	v_fmamk_f32 v245, v126, 0x3dd53b94, v178
	v_fmamk_f32 v246, v127, 0x3dd53b94, v178
	v_mfma_f32_32x32x16_bf16 v[32:47], v[80:83], v[88:91], v[32:47]
	v_fma_f32 v116, v100, s54, v178
	v_fma_f32 v117, v101, s54, v178
	v_fma_f32 v118, v102, s54, v178
	v_fma_f32 v119, v103, s54, v178
	v_fma_f32 v120, v104, s54, v178
	v_fma_f32 v121, v105, s54, v178
	v_pk_fma_f32 v[122:123], v[106:107], s[54:55], v[178:179] op_sel_hi:[1,0,0]
	v_exp_f32_e32 v80, v179
	v_exp_f32_e32 v81, v180
	v_exp_f32_e32 v82, v181
	v_mfma_f32_32x32x16_bf16 v[32:47], v[84:87], v[72:75], v[32:47]
	v_exp_f32_e32 v83, v194
	v_exp_f32_e32 v84, v195
	v_exp_f32_e32 v85, v196
	v_exp_f32_e32 v86, v197
	v_exp_f32_e32 v87, v200
	v_pk_fma_f32 v[126:127], v[110:111], s[54:55], v[178:179] op_sel_hi:[1,0,0]
	v_pk_fma_f32 v[124:125], v[108:109], s[54:55], v[178:179] op_sel_hi:[1,0,0]
	v_mfma_f32_32x32x16_bf16 v[32:47], v[92:95], v[64:67], v[32:47]
	ds_read_b64_tr_b16 v[92:93], v201 offset:0x600
	ds_read_b64_tr_b16 v[94:95], v201 offset:0xe00
	v_mfma_f32_32x32x16_bf16 v[32:47], v[112:115], v[68:71], v[32:47]
	v_fma_f32 v112, v96, s54, v178
	v_fma_f32 v113, v97, s54, v178
	ds_read_b64_tr_b16 v[96:97], v201 offset:0x1600
	v_fma_f32 v114, v98, s54, v178
	v_fma_f32 v115, v99, s54, v178
	ds_read_b64_tr_b16 v[98:99], v201 offset:0x1e00
	ds_read_b64_tr_b16 v[100:101], v201 offset:0x2600
	ds_read_b64_tr_b16 v[102:103], v201 offset:0x2e00
	ds_read_b64_tr_b16 v[104:105], v201 offset:0x3600
	ds_read_b64_tr_b16 v[106:107], v201 offset:0x3e00
	s_waitcnt lgkmcnt(0)
	v_mfma_f32_32x32x16_bf16 v[16:31], v[92:95], v[88:91], v[16:31]
	v_exp_f32_e32 v88, v239
	v_exp_f32_e32 v89, v240
	v_exp_f32_e32 v90, v241
	v_exp_f32_e32 v91, v242
	v_exp_f32_e32 v92, v243
	v_exp_f32_e32 v93, v244
	v_exp_f32_e32 v94, v245
	v_mfma_f32_32x32x16_bf16 v[16:31], v[96:99], v[72:75], v[16:31]
	v_exp_f32_e32 v95, v246
	s_barrier
	s_waitcnt vmcnt(0)
	v_cmp_gt_f32_e32 vcc, 1.0, v202
	v_mfma_f32_32x32x16_bf16 v[16:31], v[100:103], v[64:67], v[16:31]
	v_add_u32_e32 v64, 0x10000, v228
	s_waitcnt vmcnt(2)
	ds_write_b128 v205, v[76:79]
	ds_write_b128 v206, v[162:165]
	ds_write_b128 v207, v[166:169] offset:32768
	s_waitcnt vmcnt(1)
	ds_write_b128 v208, v[174:177] offset:32768
	s_waitcnt vmcnt(0)
	ds_write_b128 v64, v[170:173]
	v_mfma_f32_32x32x16_bf16 v[16:31], v[104:107], v[68:71], v[16:31]
	s_cbranch_vccz .LBB0_863
	v_pk_mul_f32 v[14:15], v[14:15], v[202:203] op_sel_hi:[1,0]
	v_pk_mul_f32 v[12:13], v[12:13], v[202:203] op_sel_hi:[1,0]
	v_pk_mul_f32 v[10:11], v[10:11], v[202:203] op_sel_hi:[1,0]
	v_pk_mul_f32 v[8:9], v[8:9], v[202:203] op_sel_hi:[1,0]
	v_pk_mul_f32 v[6:7], v[6:7], v[202:203] op_sel_hi:[1,0]
	v_pk_mul_f32 v[4:5], v[4:5], v[202:203] op_sel_hi:[1,0]
	v_pk_mul_f32 v[2:3], v[2:3], v[202:203] op_sel_hi:[1,0]
	v_pk_mul_f32 v[0:1], v[0:1], v[202:203] op_sel_hi:[1,0]
	v_pk_mul_f32 v[62:63], v[62:63], v[202:203] op_sel_hi:[1,0]
	v_pk_mul_f32 v[60:61], v[60:61], v[202:203] op_sel_hi:[1,0]
	v_pk_mul_f32 v[58:59], v[58:59], v[202:203] op_sel_hi:[1,0]
	v_pk_mul_f32 v[56:57], v[56:57], v[202:203] op_sel_hi:[1,0]
	v_pk_mul_f32 v[54:55], v[54:55], v[202:203] op_sel_hi:[1,0]
	v_pk_mul_f32 v[52:53], v[52:53], v[202:203] op_sel_hi:[1,0]
	v_pk_mul_f32 v[50:51], v[50:51], v[202:203] op_sel_hi:[1,0]
	v_pk_mul_f32 v[48:49], v[48:49], v[202:203] op_sel_hi:[1,0]
	v_pk_mul_f32 v[46:47], v[202:203], v[46:47] op_sel_hi:[0,1]
	v_pk_mul_f32 v[44:45], v[202:203], v[44:45] op_sel_hi:[0,1]
	v_pk_mul_f32 v[42:43], v[202:203], v[42:43] op_sel_hi:[0,1]
	v_pk_mul_f32 v[40:41], v[202:203], v[40:41] op_sel_hi:[0,1]
	v_pk_mul_f32 v[38:39], v[202:203], v[38:39] op_sel_hi:[0,1]
	v_pk_mul_f32 v[36:37], v[202:203], v[36:37] op_sel_hi:[0,1]
	v_pk_mul_f32 v[34:35], v[202:203], v[34:35] op_sel_hi:[0,1]
	v_pk_mul_f32 v[32:33], v[202:203], v[32:33] op_sel_hi:[0,1]
	v_pk_mul_f32 v[30:31], v[202:203], v[30:31] op_sel_hi:[0,1]
	v_pk_mul_f32 v[28:29], v[202:203], v[28:29] op_sel_hi:[0,1]
	v_pk_mul_f32 v[26:27], v[202:203], v[26:27] op_sel_hi:[0,1]
	v_pk_mul_f32 v[24:25], v[202:203], v[24:25] op_sel_hi:[0,1]
	v_pk_mul_f32 v[22:23], v[202:203], v[22:23] op_sel_hi:[0,1]
	v_pk_mul_f32 v[20:21], v[202:203], v[20:21] op_sel_hi:[0,1]
	v_pk_mul_f32 v[18:19], v[202:203], v[18:19] op_sel_hi:[0,1]
	v_pk_mul_f32 v[16:17], v[202:203], v[16:17] op_sel_hi:[0,1]
.LBB0_863:
	s_waitcnt lgkmcnt(0)
	s_barrier
	ds_read_b128 v[64:67], v209 offset:32768
	ds_read_b128 v[68:71], v209 offset:40960
	ds_read_b128 v[162:165], v211 offset:32768
	ds_read_b128 v[166:169], v211 offset:40960
	v_exp_f32_e32 v112, v112
	v_exp_f32_e32 v113, v113
	s_waitcnt lgkmcnt(3)
	v_mfma_f32_32x32x16_bf16 v[96:111], v[64:67], v[158:161], 0
	v_exp_f32_e32 v114, v114
	v_exp_f32_e32 v115, v115
	v_exp_f32_e32 v116, v116
	v_exp_f32_e32 v117, v117
	v_exp_f32_e32 v118, v118
	v_exp_f32_e32 v119, v119
	s_waitcnt lgkmcnt(2)
	v_mfma_f32_32x32x16_bf16 v[64:79], v[68:71], v[158:161], 0
	s_waitcnt lgkmcnt(1)
	v_mfma_f32_32x32x16_bf16 v[96:111], v[162:165], v[154:157], v[96:111]
	s_waitcnt lgkmcnt(0)
	v_mfma_f32_32x32x16_bf16 v[64:79], v[166:169], v[154:157], v[64:79]
	ds_read_b128 v[162:165], v212 offset:32768
	ds_read_b128 v[166:169], v212 offset:40960
	s_waitcnt lgkmcnt(1)
	v_mfma_f32_32x32x16_bf16 v[96:111], v[162:165], v[150:153], v[96:111]
	s_waitcnt lgkmcnt(0)
	v_mfma_f32_32x32x16_bf16 v[64:79], v[166:169], v[150:153], v[64:79]
	ds_read_b128 v[162:165], v213 offset:32768
	ds_read_b128 v[166:169], v213 offset:40960
	s_waitcnt lgkmcnt(1)
	v_mfma_f32_32x32x16_bf16 v[96:111], v[162:165], v[146:149], v[96:111]
	s_waitcnt lgkmcnt(0)
	v_mfma_f32_32x32x16_bf16 v[64:79], v[166:169], v[146:149], v[64:79]
	ds_read_b128 v[162:165], v215 offset:32768
	ds_read_b128 v[166:169], v215 offset:40960
	s_waitcnt lgkmcnt(1)
	v_mfma_f32_32x32x16_bf16 v[96:111], v[162:165], v[142:145], v[96:111]
	s_waitcnt lgkmcnt(0)
	v_mfma_f32_32x32x16_bf16 v[64:79], v[166:169], v[142:145], v[64:79]
	ds_read_b128 v[162:165], v217 offset:32768
	ds_read_b128 v[166:169], v217 offset:40960
	s_waitcnt lgkmcnt(1)
	v_mfma_f32_32x32x16_bf16 v[96:111], v[162:165], v[138:141], v[96:111]
	s_waitcnt lgkmcnt(0)
	v_mfma_f32_32x32x16_bf16 v[64:79], v[166:169], v[138:141], v[64:79]
	ds_read_b128 v[162:165], v214 offset:32768
	ds_read_b128 v[166:169], v214 offset:40960
	s_waitcnt lgkmcnt(1)
	v_mfma_f32_32x32x16_bf16 v[96:111], v[162:165], v[134:137], v[96:111]
	s_waitcnt lgkmcnt(0)
	v_mfma_f32_32x32x16_bf16 v[64:79], v[166:169], v[134:137], v[64:79]
	ds_read_b128 v[162:165], v216 offset:32768
	ds_read_b128 v[166:169], v216 offset:40960
	s_waitcnt lgkmcnt(1)
	v_mfma_f32_32x32x16_bf16 v[96:111], v[162:165], v[130:133], v[96:111]
	s_waitcnt lgkmcnt(0)
	v_mfma_f32_32x32x16_bf16 v[64:79], v[166:169], v[130:133], v[64:79]
	ds_read_b128 v[162:165], v219
	ds_read_b128 v[166:169], v219 offset:4096
	ds_read_b128 v[170:173], v204
	s_waitcnt lgkmcnt(0)
	v_mfma_f32_32x32x16_bf16 v[96:111], v[162:165], v[170:173], v[96:111]
	v_mfma_f32_32x32x16_bf16 v[64:79], v[166:169], v[170:173], v[64:79]
	ds_read_b128 v[162:165], v221
	ds_read_b128 v[166:169], v221 offset:4096
	ds_read_b128 v[170:173], v204 offset:1024
	s_waitcnt lgkmcnt(0)
	v_mfma_f32_32x32x16_bf16 v[96:111], v[162:165], v[170:173], v[96:111]
	v_mfma_f32_32x32x16_bf16 v[64:79], v[166:169], v[170:173], v[64:79]
	ds_read_b128 v[162:165], v223
	ds_read_b128 v[166:169], v223 offset:4096
	ds_read_b128 v[170:173], v204 offset:2048
	s_waitcnt lgkmcnt(0)
	v_mfma_f32_32x32x16_bf16 v[96:111], v[162:165], v[170:173], v[96:111]
	v_mfma_f32_32x32x16_bf16 v[64:79], v[166:169], v[170:173], v[64:79]
	ds_read_b128 v[162:165], v225
	ds_read_b128 v[166:169], v225 offset:4096
	ds_read_b128 v[170:173], v204 offset:3072
	s_waitcnt lgkmcnt(0)
	v_mfma_f32_32x32x16_bf16 v[96:111], v[162:165], v[170:173], v[96:111]
	v_exp_f32_e32 v162, v120
	v_exp_f32_e32 v163, v121
	v_exp_f32_e32 v164, v122
	v_exp_f32_e32 v165, v123
	v_add_f32_e32 v120, v80, v81
	v_add_f32_e32 v121, v88, v89
	v_add_f32_e32 v122, v112, v113
	v_mfma_f32_32x32x16_bf16 v[64:79], v[166:169], v[170:173], v[64:79]
	v_exp_f32_e32 v166, v124
	v_exp_f32_e32 v167, v125
	v_add_f32_e32 v123, v162, v163
	v_exp_f32_e32 v168, v126
	v_add_f32_e32 v120, v82, v120
	v_add_f32_e32 v121, v90, v121
	v_add_f32_e32 v122, v114, v122
	v_add_f32_e32 v123, v164, v123
	v_exp_f32_e32 v169, v127
	v_add_f32_e32 v120, v83, v120
	v_add_f32_e32 v121, v91, v121
	v_add_f32_e32 v122, v115, v122
	v_add_f32_e32 v123, v165, v123
	v_add_f32_e32 v120, v84, v120
	v_add_f32_e32 v121, v92, v121
	v_add_f32_e32 v122, v116, v122
	v_add_f32_e32 v123, v166, v123
	v_add_f32_e32 v120, v85, v120
	v_add_f32_e32 v121, v93, v121
	v_add_f32_e32 v122, v117, v122
	v_add_f32_e32 v123, v167, v123
	v_add_f32_e32 v120, v86, v120
	v_add_f32_e32 v121, v94, v121
	v_add_f32_e32 v122, v118, v122
	v_add_f32_e32 v123, v168, v123
	v_add_f32_e32 v120, v87, v120
	v_add_f32_e32 v121, v95, v121
	v_add_f32_e32 v122, v119, v122
	v_add_f32_e32 v123, v169, v123
	v_add_f32_e32 v120, v121, v120
	v_add_f32_e32 v121, v123, v122
	v_add_f32_e32 v239, v120, v121
	v_mov_b32_e32 v240, v239
	s_nop 1
	v_permlane32_swap_b32_e32 v239, v240
	v_cvt_pk_bf16_f32 v124, v80, v81
	v_cvt_pk_bf16_f32 v125, v82, v83
	v_cvt_pk_bf16_f32 v126, v84, v85
	v_cvt_pk_bf16_f32 v127, v86, v87
	v_cvt_pk_bf16_f32 v120, v88, v89
	v_cvt_pk_bf16_f32 v121, v90, v91
	v_cvt_pk_bf16_f32 v122, v92, v93
	v_cvt_pk_bf16_f32 v123, v94, v95
	v_cvt_pk_bf16_f32 v112, v112, v113
	v_cvt_pk_bf16_f32 v113, v114, v115
	v_cvt_pk_bf16_f32 v114, v116, v117
	v_cvt_pk_bf16_f32 v115, v118, v119
	v_cvt_pk_bf16_f32 v116, v162, v163
	v_cvt_pk_bf16_f32 v117, v164, v165
	v_cvt_pk_bf16_f32 v118, v166, v167
	v_cvt_pk_bf16_f32 v119, v168, v169
	s_add_i32 s2, s20, 1
	s_min_i32 s2, s2, s23
	s_lshl_b32 s72, s2, 6
	s_mul_i32 s2, s72, s62
	s_mov_b32 s3, s73
	s_lshl_b64 s[2:3], s[2:3], 1
	s_add_u32 s24, s18, s2
	s_addc_u32 s25, s19, s3
	s_add_u32 s2, s16, s2
	s_addc_u32 s3, s17, s3
	global_load_dwordx4 v[162:165], v128, s[24:25]
	global_load_dwordx4 v[166:169], v182, s[24:25]
	global_load_dwordx4 v[170:173], v128, s[2:3]
	global_load_dwordx4 v[174:177], v182, s[2:3]
	s_lshl_b64 s[2:3], s[72:73], 7
	v_lshl_add_u64 v[80:81], v[184:185], 0, s[2:3]
	global_load_dwordx4 v[178:181], v[80:81], off
	ds_read_b64_tr_b16 v[80:81], v203 offset:0
	ds_read_b64_tr_b16 v[82:83], v203 offset:0x800
	ds_read_b64_tr_b16 v[84:85], v203 offset:0x1000
	ds_read_b64_tr_b16 v[86:87], v203 offset:0x1800
	ds_read_b64_tr_b16 v[88:89], v203 offset:0x2000
	ds_read_b64_tr_b16 v[90:91], v203 offset:0x2800
	ds_read_b64_tr_b16 v[92:93], v203 offset:0x3000
	ds_read_b64_tr_b16 v[94:95], v203 offset:0x3800
	s_waitcnt lgkmcnt(0)
	s_nop 0
	v_mfma_f32_32x32x16_bf16 v[0:15], v[80:83], v[124:127], v[0:15]
	v_max_f32_e32 v80, v64, v65
	v_max3_f32 v81, v96, v97, v98
	v_max3_f32 v80, v80, v66, v67
	v_max3_f32 v81, v81, v99, v100
	v_max3_f32 v80, v80, v68, v69
	v_mfma_f32_32x32x16_bf16 v[0:15], v[84:87], v[120:123], v[0:15]
	v_max3_f32 v81, v81, v101, v102
	v_max3_f32 v80, v80, v70, v71
	v_max3_f32 v81, v81, v103, v104
	v_max3_f32 v80, v80, v72, v73
	v_max3_f32 v81, v81, v105, v106
	v_max3_f32 v80, v80, v74, v75
	v_max3_f32 v81, v81, v107, v108
	v_mfma_f32_32x32x16_bf16 v[0:15], v[88:91], v[112:115], v[0:15]
	v_max3_f32 v80, v80, v76, v77
	v_max3_f32 v81, v81, v109, v110
	v_max3_f32 v80, v80, v78, v79
	v_max3_f32 v194, v81, v111, v80
	ds_read_b64_tr_b16 v[80:81], v203 offset:0x200
	ds_read_b64_tr_b16 v[82:83], v203 offset:0xa00
	ds_read_b64_tr_b16 v[84:85], v203 offset:0x1200
	v_mfma_f32_32x32x16_bf16 v[0:15], v[92:95], v[116:119], v[0:15]
	ds_read_b64_tr_b16 v[86:87], v203 offset:0x1a00
	ds_read_b64_tr_b16 v[88:89], v203 offset:0x2200
	ds_read_b64_tr_b16 v[90:91], v203 offset:0x2a00
	ds_read_b64_tr_b16 v[92:93], v203 offset:0x3200
	ds_read_b64_tr_b16 v[94:95], v203 offset:0x3a00
	s_waitcnt lgkmcnt(0)
	v_mfma_f32_32x32x16_bf16 v[48:63], v[80:83], v[124:127], v[48:63]
	v_mov_b32_e32 v80, v194
	s_nop 1
	v_permlane32_swap_b32_e32 v194, v80
	v_max_f32_e32 v80, v194, v80
	v_sub_f32_e32 v81, v80, v227
	v_mfma_f32_32x32x16_bf16 v[48:63], v[84:87], v[120:123], v[48:63]
	v_cmp_ge_f32_e32 vcc, s34, v81
	v_mov_b32_e32 v200, 1.0
	s_cmp_eq_u64 vcc, exec
	s_cbranch_scc0 .Lmla_resc_1
.Lmla_resc_back_1:
	v_mfma_f32_32x32x16_bf16 v[48:63], v[88:91], v[112:115], v[48:63]
	ds_read_b64_tr_b16 v[80:81], v203 offset:0x400
	ds_read_b64_tr_b16 v[82:83], v203 offset:0xc00
	ds_read_b64_tr_b16 v[84:85], v203 offset:0x1400
	ds_read_b64_tr_b16 v[86:87], v203 offset:0x1c00
	v_mfma_f32_32x32x16_bf16 v[48:63], v[92:95], v[116:119], v[48:63]
	ds_read_b64_tr_b16 v[88:89], v203 offset:0x2400
	ds_read_b64_tr_b16 v[90:91], v203 offset:0x2c00
	ds_read_b64_tr_b16 v[92:93], v203 offset:0x3400
	ds_read_b64_tr_b16 v[94:95], v203 offset:0x3c00
	s_waitcnt lgkmcnt(0)
	v_mul_f32_e32 v242, 0xbdd53b94, v227
	v_fmamk_f32 v96, v96, 0x3dd53b94, v242
	v_fmamk_f32 v97, v97, 0x3dd53b94, v242
	v_fmamk_f32 v98, v98, 0x3dd53b94, v242
	v_fmamk_f32 v99, v99, 0x3dd53b94, v242
	v_fmamk_f32 v100, v100, 0x3dd53b94, v242
	v_fmamk_f32 v101, v101, 0x3dd53b94, v242
	v_fmamk_f32 v102, v102, 0x3dd53b94, v242
	v_fmamk_f32 v103, v103, 0x3dd53b94, v242
	v_fmamk_f32 v194, v104, 0x3dd53b94, v242
	v_fmamk_f32 v195, v105, 0x3dd53b94, v242
	v_fmamk_f32 v196, v106, 0x3dd53b94, v242
	v_fmamk_f32 v197, v107, 0x3dd53b94, v242
	v_fmamk_f32 v108, v108, 0x3dd53b94, v242
	v_fmamk_f32 v109, v109, 0x3dd53b94, v242
	v_fmamk_f32 v110, v110, 0x3dd53b94, v242
	v_fmamk_f32 v111, v111, 0x3dd53b94, v242
	v_mfma_f32_32x32x16_bf16 v[32:47], v[80:83], v[124:127], v[32:47]
	v_fma_f32 v80, v64, s54, v242
	v_fma_f32 v81, v65, s54, v242
	v_exp_f32_e32 v64, v96
	v_exp_f32_e32 v65, v97
	v_pk_fma_f32 v[82:83], v[66:67], s[54:55], v[242:243] op_sel_hi:[1,0,0]
	v_exp_f32_e32 v66, v98
	v_exp_f32_e32 v67, v99
	v_mfma_f32_32x32x16_bf16 v[32:47], v[84:87], v[120:123], v[32:47]
	v_fma_f32 v84, v68, s54, v242
	v_fma_f32 v85, v69, s54, v242
	v_exp_f32_e32 v68, v100
	v_exp_f32_e32 v69, v101
	v_pk_fma_f32 v[86:87], v[70:71], s[54:55], v[242:243] op_sel_hi:[1,0,0]
	v_exp_f32_e32 v70, v102
	v_exp_f32_e32 v71, v103
	v_mfma_f32_32x32x16_bf16 v[32:47], v[88:91], v[112:115], v[32:47]
	v_fma_f32 v88, v72, s54, v242
	v_fma_f32 v89, v73, s54, v242
	ds_read_b64_tr_b16 v[72:73], v203 offset:0x600
	v_fma_f32 v90, v74, s54, v242
	v_fma_f32 v91, v75, s54, v242
	ds_read_b64_tr_b16 v[74:75], v203 offset:0xe00
	ds_read_b64_tr_b16 v[96:97], v203 offset:0x1600
	ds_read_b64_tr_b16 v[98:99], v203 offset:0x1e00
	ds_read_b64_tr_b16 v[100:101], v203 offset:0x2600
	v_mfma_f32_32x32x16_bf16 v[32:47], v[92:95], v[116:119], v[32:47]
	ds_read_b64_tr_b16 v[102:103], v203 offset:0x2e00
	ds_read_b64_tr_b16 v[104:105], v203 offset:0x3600
	ds_read_b64_tr_b16 v[106:107], v203 offset:0x3e00
	s_waitcnt lgkmcnt(0)
	v_fma_f32 v94, v78, s54, v242
	v_fma_f32 v95, v79, s54, v242
	v_fma_f32 v92, v76, s54, v242
	v_fma_f32 v93, v77, s54, v242
	v_mfma_f32_32x32x16_bf16 v[16:31], v[72:75], v[124:127], v[16:31]
	v_exp_f32_e32 v72, v194
	v_exp_f32_e32 v73, v195
	v_exp_f32_e32 v74, v196
	v_exp_f32_e32 v75, v197
	v_exp_f32_e32 v76, v108
	v_exp_f32_e32 v77, v109
	v_exp_f32_e32 v78, v110
	v_mfma_f32_32x32x16_bf16 v[16:31], v[96:99], v[120:123], v[16:31]
	v_exp_f32_e32 v79, v111
	s_barrier
	s_waitcnt vmcnt(0)
	v_cmp_gt_f32_e32 vcc, 1.0, v200
	v_mfma_f32_32x32x16_bf16 v[16:31], v[100:103], v[112:115], v[16:31]
	s_waitcnt vmcnt(4)
	ds_write_b128 v205, v[162:165] offset:16384
	s_waitcnt vmcnt(3)
	ds_write_b128 v206, v[166:169] offset:16384
	s_waitcnt vmcnt(2)
	ds_write_b128 v207, v[170:173] offset:49152
	s_waitcnt vmcnt(1)
	ds_write_b128 v208, v[174:177] offset:49152
	s_waitcnt vmcnt(0)
	ds_write_b128 v229, v[178:181]
	v_mfma_f32_32x32x16_bf16 v[16:31], v[104:107], v[116:119], v[16:31]
	s_cbranch_vccz .LBB0_865
	v_pk_mul_f32 v[14:15], v[14:15], v[200:201] op_sel_hi:[1,0]
	v_pk_mul_f32 v[12:13], v[12:13], v[200:201] op_sel_hi:[1,0]
	v_pk_mul_f32 v[10:11], v[10:11], v[200:201] op_sel_hi:[1,0]
	v_pk_mul_f32 v[8:9], v[8:9], v[200:201] op_sel_hi:[1,0]
	v_pk_mul_f32 v[6:7], v[6:7], v[200:201] op_sel_hi:[1,0]
	v_pk_mul_f32 v[4:5], v[4:5], v[200:201] op_sel_hi:[1,0]
	v_pk_mul_f32 v[2:3], v[2:3], v[200:201] op_sel_hi:[1,0]
	v_pk_mul_f32 v[0:1], v[0:1], v[200:201] op_sel_hi:[1,0]
	v_pk_mul_f32 v[62:63], v[62:63], v[200:201] op_sel_hi:[1,0]
	v_pk_mul_f32 v[60:61], v[60:61], v[200:201] op_sel_hi:[1,0]
	v_pk_mul_f32 v[58:59], v[58:59], v[200:201] op_sel_hi:[1,0]
	v_pk_mul_f32 v[56:57], v[56:57], v[200:201] op_sel_hi:[1,0]
	v_pk_mul_f32 v[54:55], v[54:55], v[200:201] op_sel_hi:[1,0]
	v_pk_mul_f32 v[52:53], v[52:53], v[200:201] op_sel_hi:[1,0]
	v_pk_mul_f32 v[50:51], v[50:51], v[200:201] op_sel_hi:[1,0]
	v_pk_mul_f32 v[48:49], v[48:49], v[200:201] op_sel_hi:[1,0]
	v_pk_mul_f32 v[46:47], v[200:201], v[46:47] op_sel_hi:[0,1]
	v_pk_mul_f32 v[44:45], v[200:201], v[44:45] op_sel_hi:[0,1]
	v_pk_mul_f32 v[42:43], v[200:201], v[42:43] op_sel_hi:[0,1]
	v_pk_mul_f32 v[40:41], v[200:201], v[40:41] op_sel_hi:[0,1]
	v_pk_mul_f32 v[38:39], v[200:201], v[38:39] op_sel_hi:[0,1]
	v_pk_mul_f32 v[36:37], v[200:201], v[36:37] op_sel_hi:[0,1]
	v_pk_mul_f32 v[34:35], v[200:201], v[34:35] op_sel_hi:[0,1]
	v_pk_mul_f32 v[32:33], v[200:201], v[32:33] op_sel_hi:[0,1]
	v_pk_mul_f32 v[30:31], v[200:201], v[30:31] op_sel_hi:[0,1]
	v_pk_mul_f32 v[28:29], v[200:201], v[28:29] op_sel_hi:[0,1]
	v_pk_mul_f32 v[26:27], v[200:201], v[26:27] op_sel_hi:[0,1]
	v_pk_mul_f32 v[24:25], v[200:201], v[24:25] op_sel_hi:[0,1]
	v_pk_mul_f32 v[22:23], v[200:201], v[22:23] op_sel_hi:[0,1]
	v_pk_mul_f32 v[20:21], v[200:201], v[20:21] op_sel_hi:[0,1]
	v_pk_mul_f32 v[18:19], v[200:201], v[18:19] op_sel_hi:[0,1]
	v_pk_mul_f32 v[16:17], v[200:201], v[16:17] op_sel_hi:[0,1]

.Lmla_resc_1:
	v_max_f32_e32 v80, v227, v80
	v_sub_f32_e32 v81, v227, v80
	v_mul_f32_e32 v81, 0x3dd53b94, v81
	v_exp_f32_e32 v81, v81
	s_nop 0
	v_mov_b32_e32 v200, v81
	v_mov_b32_e32 v227, v80
	s_branch .Lmla_resc_back_1
.Lmla_resc_0:
	v_max_f32_e32 v80, v227, v80
	v_sub_f32_e32 v81, v227, v80
	v_mul_f32_e32 v81, 0x3dd53b94, v81
	v_exp_f32_e32 v81, v81
	s_nop 0
	v_mov_b32_e32 v202, v81
	v_mov_b32_e32 v227, v80
	s_branch .Lmla_resc_back_0
